# baseline (speedup 1.0000x reference)
.LBB1_29:
	v_add_f32_e32 v203, v203, v58
	v_max_f32_e32 v58, v99, v99
	v_max_f32_e32 v59, v98, v98
	v_max_f32_e32 v58, v59, v58
	v_max3_f32 v59, v100, v101, v83
	v_max3_f32 v58, v58, v82, v84
	v_max3_f32 v58, v58, v85, v102
	v_max3_f32 v59, v59, v104, v105
	v_max3_f32 v58, v58, v103, v86
	v_max3_f32 v59, v59, v88, v89
	v_max3_f32 v58, v58, v87, v106
	v_max3_f32 v59, v59, v108, v109
	v_max3_f32 v58, v58, v107, v90
	v_max3_f32 v59, v59, v92, v93
	v_max3_f32 v58, v58, v91, v110
	v_max3_f32 v59, v59, v112, v113
	v_max3_f32 v58, v58, v111, v94
	v_max3_f32 v59, v59, v96, v97
	v_max3_f32 v58, v58, v95, v59
	v_cmp_lt_f32_e32 vcc, s46, v58
	s_cmp_lg_u64 vcc, 0
	s_cselect_b64 s[2:3], -1, 0
	s_cbranch_vccnz .LBB1_67

.LBB1_40:
	v_add_f32_e32 v203, v203, v90
	v_max_f32_e32 v90, v67, v67
	v_max_f32_e32 v91, v66, v66
	v_max_f32_e32 v90, v91, v90
	v_max3_f32 v91, v68, v69, v51
	v_max3_f32 v90, v90, v50, v52
	v_max3_f32 v90, v90, v53, v70
	v_max3_f32 v91, v91, v72, v73
	v_max3_f32 v90, v90, v71, v54
	v_max3_f32 v91, v91, v56, v57
	v_max3_f32 v90, v90, v55, v74
	v_max3_f32 v91, v91, v76, v77
	v_max3_f32 v90, v90, v75, v58
	v_max3_f32 v91, v91, v60, v61
	v_max3_f32 v90, v90, v59, v78
	v_max3_f32 v91, v91, v80, v81
	v_max3_f32 v90, v90, v79, v62
	v_max3_f32 v91, v91, v64, v65
	v_max3_f32 v90, v90, v63, v91
	v_cmp_lt_f32_e32 vcc, s46, v90
	s_cmp_lg_u64 vcc, 0
	s_cselect_b64 s[24:25], -1, 0
	s_cbranch_vccnz .LBB1_70

.LBB1_67:
	v_mov_b32_e32 v59, v58
	s_nop 1
	v_permlane32_swap_b32_e32 v58, v59
	v_max_f32_e32 v59, v59, v59
	v_max_f32_e32 v58, v58, v58
	v_max_f32_e32 v58, v58, v59
	v_max_f32_e32 v34, v58, v58
	v_max_f32_e32 v58, 0, v34
	v_exp_f32_e64 v59, -v58
	v_add_f32_e32 v199, v199, v58
	v_xor_b32_e32 v34, 0x80000000, v199
	v_mov_b32_e32 v35, v34
	v_mov_b32_e32 v36, v34
	v_mov_b32_e32 v37, v34
	v_mov_b32_e32 v38, v34
	v_mov_b32_e32 v39, v34
	v_mov_b32_e32 v40, v34
	v_mov_b32_e32 v41, v34
	v_mov_b32_e32 v42, v34
	v_mov_b32_e32 v43, v34
	v_mov_b32_e32 v44, v34
	v_mov_b32_e32 v45, v34
	v_mov_b32_e32 v46, v34
	v_mov_b32_e32 v47, v34
	v_mov_b32_e32 v48, v34
	v_mov_b32_e32 v49, v34
	s_and_saveexec_b64 s[22:23], s[0:1]
	ds_write_b32 v198, v59 offset:49152
	s_or_b64 exec, exec, s[22:23]
	v_sub_f32_e32 v113, v113, v58
	v_sub_f32_e32 v112, v112, v58
	v_sub_f32_e32 v111, v111, v58
	v_sub_f32_e32 v110, v110, v58
	v_sub_f32_e32 v109, v109, v58
	v_sub_f32_e32 v108, v108, v58
	v_sub_f32_e32 v107, v107, v58
	v_sub_f32_e32 v106, v106, v58
	v_sub_f32_e32 v105, v105, v58
	v_sub_f32_e32 v104, v104, v58
	v_sub_f32_e32 v103, v103, v58
	v_sub_f32_e32 v102, v102, v58
	v_sub_f32_e32 v101, v101, v58
	v_sub_f32_e32 v100, v100, v58
	v_sub_f32_e32 v99, v99, v58
	v_sub_f32_e32 v98, v98, v58
	v_sub_f32_e32 v97, v97, v58
	v_sub_f32_e32 v96, v96, v58
	v_sub_f32_e32 v95, v95, v58
	v_sub_f32_e32 v94, v94, v58
	v_sub_f32_e32 v93, v93, v58
	v_sub_f32_e32 v92, v92, v58
	v_sub_f32_e32 v91, v91, v58
	v_sub_f32_e32 v90, v90, v58
	v_sub_f32_e32 v89, v89, v58
	v_sub_f32_e32 v88, v88, v58
	v_sub_f32_e32 v87, v87, v58
	v_sub_f32_e32 v86, v86, v58
	v_sub_f32_e32 v85, v85, v58
	v_sub_f32_e32 v84, v84, v58
	v_sub_f32_e32 v83, v83, v58
	v_sub_f32_e32 v82, v82, v58
	v_mul_f32_e32 v203, v203, v59
	s_branch .LBB1_30
.LBB1_70:
	v_mov_b32_e32 v91, v90
	s_nop 1
	v_permlane32_swap_b32_e32 v90, v91
	v_max_f32_e32 v91, v91, v91
	v_max_f32_e32 v90, v90, v90
	v_max_f32_e32 v90, v90, v91
	v_max_f32_e32 v34, v90, v90
	v_max_f32_e32 v90, 0, v34
	v_exp_f32_e64 v91, -v90
	v_add_f32_e32 v199, v199, v90
	v_xor_b32_e32 v34, 0x80000000, v199
	v_mov_b32_e32 v35, v34
	v_mov_b32_e32 v36, v34
	v_mov_b32_e32 v37, v34
	v_mov_b32_e32 v38, v34
	v_mov_b32_e32 v39, v34
	v_mov_b32_e32 v40, v34
	v_mov_b32_e32 v41, v34
	v_mov_b32_e32 v42, v34
	v_mov_b32_e32 v43, v34
	v_mov_b32_e32 v44, v34
	v_mov_b32_e32 v45, v34
	v_mov_b32_e32 v46, v34
	v_mov_b32_e32 v47, v34
	v_mov_b32_e32 v48, v34
	v_mov_b32_e32 v49, v34
	s_and_saveexec_b64 s[2:3], s[0:1]
	ds_write_b32 v198, v91 offset:49152
	s_or_b64 exec, exec, s[2:3]
	v_sub_f32_e32 v81, v81, v90
	v_sub_f32_e32 v80, v80, v90
	v_sub_f32_e32 v79, v79, v90
	v_sub_f32_e32 v78, v78, v90
	v_sub_f32_e32 v77, v77, v90
	v_sub_f32_e32 v76, v76, v90
	v_sub_f32_e32 v75, v75, v90
	v_sub_f32_e32 v74, v74, v90
	v_sub_f32_e32 v73, v73, v90
	v_sub_f32_e32 v72, v72, v90
	v_sub_f32_e32 v71, v71, v90
	v_sub_f32_e32 v70, v70, v90
	v_sub_f32_e32 v69, v69, v90
	v_sub_f32_e32 v68, v68, v90
	v_sub_f32_e32 v67, v67, v90
	v_sub_f32_e32 v66, v66, v90
	v_sub_f32_e32 v65, v65, v90
	v_sub_f32_e32 v64, v64, v90
	v_sub_f32_e32 v63, v63, v90
	v_sub_f32_e32 v62, v62, v90
	v_sub_f32_e32 v61, v61, v90
	v_sub_f32_e32 v60, v60, v90
	v_sub_f32_e32 v59, v59, v90
	v_sub_f32_e32 v58, v58, v90
	v_sub_f32_e32 v57, v57, v90
	v_sub_f32_e32 v56, v56, v90
	v_sub_f32_e32 v55, v55, v90
	v_sub_f32_e32 v54, v54, v90
	v_sub_f32_e32 v53, v53, v90
	v_sub_f32_e32 v52, v52, v90
	v_sub_f32_e32 v51, v51, v90
	v_sub_f32_e32 v50, v50, v90
	v_mul_f32_e32 v203, v203, v91
	s_branch .LBB1_41

.Lmend_0f:
	v_max_f32_e32 v67, v51, v51
	v_max_f32_e32 v67, v68, v67
	v_max3_f32 v68, v52, v53, v35
	v_max3_f32 v67, v67, v34, v36
	v_max3_f32 v67, v67, v37, v54
	v_max3_f32 v68, v68, v56, v57
	v_max3_f32 v67, v67, v55, v38
	v_max3_f32 v68, v68, v40, v41
	v_max3_f32 v67, v67, v39, v58
	v_max3_f32 v68, v68, v60, v61
	v_max3_f32 v67, v67, v59, v42
	v_max3_f32 v68, v68, v44, v45
	v_max3_f32 v67, v67, v43, v62
	v_max3_f32 v68, v68, v64, v65
	v_max3_f32 v67, v67, v63, v46
	v_max3_f32 v68, v68, v48, v49
	v_max3_f32 v66, v67, v47, v68
	v_cmp_lt_f32_e32 vcc, s2, v66
	s_cmp_lg_u64 vcc, 0
	s_cselect_b64 s[2:3], -1, 0
	s_cbranch_vccnz .LBB1_160

.Lmend_1f:
	v_max_f32_e32 v66, v49, v49
	v_max_f32_e32 v66, v67, v66
	v_max3_f32 v67, v50, v51, v33
	v_max3_f32 v66, v66, v32, v34
	v_max3_f32 v66, v66, v35, v52
	v_max3_f32 v67, v67, v54, v55
	v_max3_f32 v66, v66, v53, v36
	v_max3_f32 v67, v67, v38, v39
	v_max3_f32 v66, v66, v37, v56
	v_max3_f32 v67, v67, v58, v59
	v_max3_f32 v66, v66, v57, v40
	v_max3_f32 v67, v67, v42, v43
	v_max3_f32 v66, v66, v41, v60
	v_max3_f32 v67, v67, v62, v63
	v_max3_f32 v66, v66, v61, v44
	v_max3_f32 v67, v67, v46, v47
	v_max3_f32 v64, v66, v45, v67
	v_cmp_lt_f32_e32 vcc, s2, v64
	s_cmp_lg_u64 vcc, 0
	s_cselect_b64 s[2:3], -1, 0
	s_cbranch_vccnz .LBB1_163

.LBB1_116:
	v_add_f32_e32 v64, v64, v56
	v_max_f32_e32 v56, v113, v113
	v_max_f32_e32 v57, v112, v112
	v_max_f32_e32 v56, v57, v56
	v_max3_f32 v57, v114, v115, v97
	v_max3_f32 v56, v56, v96, v98
	v_max3_f32 v56, v56, v99, v116
	v_max3_f32 v57, v57, v118, v119
	v_max3_f32 v56, v56, v117, v100
	v_max3_f32 v57, v57, v102, v103
	v_max3_f32 v56, v56, v101, v120
	v_max3_f32 v57, v57, v122, v123
	v_max3_f32 v56, v56, v121, v104
	v_max3_f32 v57, v57, v106, v107
	v_max3_f32 v56, v56, v105, v124
	v_max3_f32 v57, v57, v126, v127
	v_max3_f32 v56, v56, v125, v108
	v_max3_f32 v57, v57, v110, v111
	v_max3_f32 v56, v56, v109, v57
	v_cmp_lt_f32_e32 vcc, s30, v56
	s_cmp_lg_u64 vcc, 0
	s_cselect_b64 s[2:3], -1, 0
	s_cbranch_vccnz .LBB1_154

.LBB1_127:
	v_add_f32_e32 v64, v64, v79
	v_max_f32_e32 v79, v81, v81
	v_max_f32_e32 v96, v80, v80
	v_max_f32_e32 v79, v96, v79
	v_max3_f32 v96, v82, v83, v49
	v_max3_f32 v79, v79, v48, v50
	v_max3_f32 v79, v79, v51, v84
	v_max3_f32 v96, v96, v86, v87
	v_max3_f32 v79, v79, v85, v52
	v_max3_f32 v96, v96, v54, v55
	v_max3_f32 v79, v79, v53, v88
	v_max3_f32 v96, v96, v90, v91
	v_max3_f32 v79, v79, v89, v56
	v_max3_f32 v96, v96, v58, v59
	v_max3_f32 v79, v79, v57, v92
	v_max3_f32 v96, v96, v94, v95
	v_max3_f32 v79, v79, v93, v60
	v_max3_f32 v96, v96, v62, v63
	v_max3_f32 v79, v79, v61, v96
	v_cmp_lt_f32_e32 vcc, s30, v79
	s_cmp_lg_u64 vcc, 0
	s_cselect_b64 s[14:15], -1, 0
	s_cbranch_vccnz .LBB1_157

.LBB1_154:
	v_mov_b32_e32 v57, v56
	s_nop 1
	v_permlane32_swap_b32_e32 v56, v57
	v_max_f32_e32 v57, v57, v57
	v_max_f32_e32 v56, v56, v56
	v_max_f32_e32 v56, v56, v57
	v_max_f32_e32 v32, v56, v56
	v_max_f32_e32 v56, 0, v32
	v_exp_f32_e64 v57, -v56
	v_add_f32_e32 v249, v249, v56
	v_xor_b32_e32 v32, 0x80000000, v249
	v_mov_b32_e32 v33, v32
	v_mov_b32_e32 v34, v32
	v_mov_b32_e32 v35, v32
	v_mov_b32_e32 v36, v32
	v_mov_b32_e32 v37, v32
	v_mov_b32_e32 v38, v32
	v_mov_b32_e32 v39, v32
	v_mov_b32_e32 v40, v32
	v_mov_b32_e32 v41, v32
	v_mov_b32_e32 v42, v32
	v_mov_b32_e32 v43, v32
	v_mov_b32_e32 v44, v32
	v_mov_b32_e32 v45, v32
	v_mov_b32_e32 v46, v32
	v_mov_b32_e32 v47, v32
	s_and_saveexec_b64 s[12:13], s[0:1]
	ds_write_b32 v205, v57 offset:49152
	s_or_b64 exec, exec, s[12:13]
	v_sub_f32_e32 v127, v127, v56
	v_sub_f32_e32 v126, v126, v56
	v_sub_f32_e32 v125, v125, v56
	v_sub_f32_e32 v124, v124, v56
	v_sub_f32_e32 v123, v123, v56
	v_sub_f32_e32 v122, v122, v56
	v_sub_f32_e32 v121, v121, v56
	v_sub_f32_e32 v120, v120, v56
	v_sub_f32_e32 v119, v119, v56
	v_sub_f32_e32 v118, v118, v56
	v_sub_f32_e32 v117, v117, v56
	v_sub_f32_e32 v116, v116, v56
	v_sub_f32_e32 v115, v115, v56
	v_sub_f32_e32 v114, v114, v56
	v_sub_f32_e32 v113, v113, v56
	v_sub_f32_e32 v112, v112, v56
	v_sub_f32_e32 v111, v111, v56
	v_sub_f32_e32 v110, v110, v56
	v_sub_f32_e32 v109, v109, v56
	v_sub_f32_e32 v108, v108, v56
	v_sub_f32_e32 v107, v107, v56
	v_sub_f32_e32 v106, v106, v56
	v_sub_f32_e32 v105, v105, v56
	v_sub_f32_e32 v104, v104, v56
	v_sub_f32_e32 v103, v103, v56
	v_sub_f32_e32 v102, v102, v56
	v_sub_f32_e32 v101, v101, v56
	v_sub_f32_e32 v100, v100, v56
	v_sub_f32_e32 v99, v99, v56
	v_sub_f32_e32 v98, v98, v56
	v_sub_f32_e32 v97, v97, v56
	v_sub_f32_e32 v96, v96, v56
	v_mul_f32_e32 v64, v64, v57
	s_branch .LBB1_117
.LBB1_157:
	v_mov_b32_e32 v96, v79
	s_nop 1
	v_permlane32_swap_b32_e32 v79, v96
	v_max_f32_e32 v96, v96, v96
	v_max_f32_e32 v79, v79, v79
	v_max_f32_e32 v79, v79, v96
	v_max_f32_e32 v32, v79, v79
	v_max_f32_e32 v79, 0, v32
	v_exp_f32_e64 v96, -v79
	v_add_f32_e32 v249, v249, v79
	v_xor_b32_e32 v32, 0x80000000, v249
	v_mov_b32_e32 v33, v32
	v_mov_b32_e32 v34, v32
	v_mov_b32_e32 v35, v32
	v_mov_b32_e32 v36, v32
	v_mov_b32_e32 v37, v32
	v_mov_b32_e32 v38, v32
	v_mov_b32_e32 v39, v32
	v_mov_b32_e32 v40, v32
	v_mov_b32_e32 v41, v32
	v_mov_b32_e32 v42, v32
	v_mov_b32_e32 v43, v32
	v_mov_b32_e32 v44, v32
	v_mov_b32_e32 v45, v32
	v_mov_b32_e32 v46, v32
	v_mov_b32_e32 v47, v32
	s_and_saveexec_b64 s[2:3], s[0:1]
	ds_write_b32 v205, v96 offset:49152
	s_or_b64 exec, exec, s[2:3]
	v_sub_f32_e32 v95, v95, v79
	v_sub_f32_e32 v94, v94, v79
	v_sub_f32_e32 v93, v93, v79
	v_sub_f32_e32 v92, v92, v79
	v_sub_f32_e32 v91, v91, v79
	v_sub_f32_e32 v90, v90, v79
	v_sub_f32_e32 v89, v89, v79
	v_sub_f32_e32 v88, v88, v79
	v_sub_f32_e32 v87, v87, v79
	v_sub_f32_e32 v86, v86, v79
	v_sub_f32_e32 v85, v85, v79
	v_sub_f32_e32 v84, v84, v79
	v_sub_f32_e32 v83, v83, v79
	v_sub_f32_e32 v82, v82, v79
	v_sub_f32_e32 v81, v81, v79
	v_sub_f32_e32 v80, v80, v79
	v_sub_f32_e32 v63, v63, v79
	v_sub_f32_e32 v62, v62, v79
	v_sub_f32_e32 v61, v61, v79
	v_sub_f32_e32 v60, v60, v79
	v_sub_f32_e32 v59, v59, v79
	v_sub_f32_e32 v58, v58, v79
	v_sub_f32_e32 v57, v57, v79
	v_sub_f32_e32 v56, v56, v79
	v_sub_f32_e32 v55, v55, v79
	v_sub_f32_e32 v54, v54, v79
	v_sub_f32_e32 v53, v53, v79
	v_sub_f32_e32 v52, v52, v79
	v_sub_f32_e32 v51, v51, v79
	v_sub_f32_e32 v50, v50, v79
	v_sub_f32_e32 v49, v49, v79
	v_sub_f32_e32 v48, v48, v79
	v_mul_f32_e32 v64, v64, v96
	s_branch .LBB1_128
.LBB1_160:
	v_mov_b32_e32 v67, v66
	s_nop 1
	v_permlane32_swap_b32_e32 v66, v67
	v_max_f32_e32 v67, v67, v67
	v_max_f32_e32 v66, v66, v66
	v_max_f32_e32 v66, v66, v67
	v_max_f32_e32 v66, v66, v66
	v_max_f32_e32 v80, 0, v66
	v_exp_f32_e64 v83, -v80
	v_add_f32_e32 v66, v199, v80
	v_xor_b32_e32 v66, 0x80000000, v66
	v_sub_f32_e32 v65, v65, v80
	v_sub_f32_e32 v64, v64, v80
	v_sub_f32_e32 v63, v63, v80
	v_sub_f32_e32 v62, v62, v80
	v_sub_f32_e32 v61, v61, v80
	v_sub_f32_e32 v60, v60, v80
	v_sub_f32_e32 v59, v59, v80
	v_sub_f32_e32 v58, v58, v80
	v_sub_f32_e32 v57, v57, v80
	v_sub_f32_e32 v56, v56, v80
	v_sub_f32_e32 v55, v55, v80
	v_sub_f32_e32 v54, v54, v80
	v_sub_f32_e32 v53, v53, v80
	v_sub_f32_e32 v52, v52, v80
	v_sub_f32_e32 v51, v51, v80
	v_sub_f32_e32 v50, v50, v80
	v_sub_f32_e32 v49, v49, v80
	v_sub_f32_e32 v48, v48, v80
	v_sub_f32_e32 v47, v47, v80
	v_sub_f32_e32 v46, v46, v80
	v_sub_f32_e32 v45, v45, v80
	v_sub_f32_e32 v44, v44, v80
	v_sub_f32_e32 v43, v43, v80
	v_sub_f32_e32 v42, v42, v80
	v_sub_f32_e32 v41, v41, v80
	v_sub_f32_e32 v40, v40, v80
	v_sub_f32_e32 v39, v39, v80
	v_sub_f32_e32 v38, v38, v80
	v_sub_f32_e32 v37, v37, v80
	v_sub_f32_e32 v36, v36, v80
	v_sub_f32_e32 v35, v35, v80
	v_sub_f32_e32 v34, v34, v80
	v_mov_b32_e32 v67, v66
	v_mov_b32_e32 v68, v66
	v_mov_b32_e32 v69, v66
	v_mov_b32_e32 v70, v66
	v_mov_b32_e32 v71, v66
	v_mov_b32_e32 v72, v66
	v_mov_b32_e32 v73, v66
	v_mov_b32_e32 v74, v66
	v_mov_b32_e32 v75, v66
	v_mov_b32_e32 v76, v66
	v_mov_b32_e32 v77, v66
	v_mov_b32_e32 v78, v66
	v_mov_b32_e32 v79, v66
	v_mov_b32_e32 v80, v66
	v_mov_b32_e32 v81, v66
	s_and_saveexec_b64 s[16:17], s[0:1]
	ds_write_b32 v198, v83 offset:49152
	s_or_b64 exec, exec, s[16:17]
	v_mul_f32_e32 v82, v82, v83
	s_branch .LBB1_75
.LBB1_163:
	v_mov_b32_e32 v65, v64
	s_nop 1
	v_permlane32_swap_b32_e32 v64, v65
	v_max_f32_e32 v65, v65, v65
	v_max_f32_e32 v64, v64, v64
	v_max_f32_e32 v64, v64, v65
	v_max_f32_e32 v64, v64, v64
	v_max_f32_e32 v78, 0, v64
	v_exp_f32_e64 v97, -v78
	v_add_f32_e32 v64, v249, v78
	v_xor_b32_e32 v64, 0x80000000, v64
	v_sub_f32_e32 v63, v63, v78
	v_sub_f32_e32 v62, v62, v78
	v_sub_f32_e32 v61, v61, v78
	v_sub_f32_e32 v60, v60, v78
	v_sub_f32_e32 v59, v59, v78
	v_sub_f32_e32 v58, v58, v78
	v_sub_f32_e32 v57, v57, v78
	v_sub_f32_e32 v56, v56, v78
	v_sub_f32_e32 v55, v55, v78
	v_sub_f32_e32 v54, v54, v78
	v_sub_f32_e32 v53, v53, v78
	v_sub_f32_e32 v52, v52, v78
	v_sub_f32_e32 v51, v51, v78
	v_sub_f32_e32 v50, v50, v78
	v_sub_f32_e32 v49, v49, v78
	v_sub_f32_e32 v48, v48, v78
	v_sub_f32_e32 v47, v47, v78
	v_sub_f32_e32 v46, v46, v78
	v_sub_f32_e32 v45, v45, v78
	v_sub_f32_e32 v44, v44, v78
	v_sub_f32_e32 v43, v43, v78
	v_sub_f32_e32 v42, v42, v78
	v_sub_f32_e32 v41, v41, v78
	v_sub_f32_e32 v40, v40, v78
	v_sub_f32_e32 v39, v39, v78
	v_sub_f32_e32 v38, v38, v78
	v_sub_f32_e32 v37, v37, v78
	v_sub_f32_e32 v36, v36, v78
	v_sub_f32_e32 v35, v35, v78
	v_sub_f32_e32 v34, v34, v78
	v_sub_f32_e32 v33, v33, v78
	v_sub_f32_e32 v32, v32, v78
	v_mov_b32_e32 v65, v64
	v_mov_b32_e32 v66, v64
	v_mov_b32_e32 v67, v64
	v_mov_b32_e32 v68, v64
	v_mov_b32_e32 v69, v64
	v_mov_b32_e32 v70, v64
	v_mov_b32_e32 v71, v64
	v_mov_b32_e32 v72, v64
	v_mov_b32_e32 v73, v64
	v_mov_b32_e32 v74, v64
	v_mov_b32_e32 v75, v64
	v_mov_b32_e32 v76, v64
	v_mov_b32_e32 v77, v64
	v_mov_b32_e32 v78, v64
	v_mov_b32_e32 v79, v64
	s_and_saveexec_b64 s[4:5], s[0:1]
	ds_write_b32 v205, v97 offset:49152
	s_or_b64 exec, exec, s[4:5]
	v_mul_f32_e32 v96, v96, v97
	s_branch .LBB1_104
